# H2 scan: next 8 chunks' loads issued before the current 8 are reduced (two register sets, counted vmcnt); MoE done-wait L1 invalidate moved before the poll
# baseline (speedup 1.0000x reference)
.LBB0_706:
	v_lshl_add_u64 v[116:117], s[16:17], 0, v[106:107]
	v_add_co_u32_e32 v4, vcc, 0x57518000, v116
	v_lshl_add_u64 v[8:9], s[16:17], 0, v[104:105]
	s_nop 0
	v_addc_co_u32_e32 v5, vcc, 0, v117, vcc
	global_load_dwordx4 v[80:83], v[4:5], off offset:1792 nt
	s_mov_b64 s[8:9], 0x5f51a900
	v_add_co_u32_e32 v6, vcc, 0x5f51a000, v8
	v_lshl_add_u64 v[4:5], v[8:9], 0, s[8:9]
	s_nop 0
	v_addc_co_u32_e32 v7, vcc, 0, v9, vcc
	global_load_dwordx4 v[100:103], v[6:7], off offset:2304
	global_load_dwordx4 v[96:99], v[4:5], off offset:16
	v_add_co_u32_e32 v4, vcc, 0x57520000, v116
	s_mov_b64 s[8:9], 0x5f51ab00
	s_nop 0
	v_addc_co_u32_e32 v5, vcc, 0, v117, vcc
	global_load_dwordx4 v[76:79], v[4:5], off offset:1792 nt
	v_lshl_add_u64 v[4:5], v[8:9], 0, s[8:9]
	global_load_dwordx4 v[92:95], v[6:7], off offset:2816
	global_load_dwordx4 v[88:91], v[4:5], off offset:16
	v_add_co_u32_e32 v4, vcc, 0x57528000, v116
	s_mov_b64 s[8:9], 0x5f51ad00
	s_nop 0
	v_addc_co_u32_e32 v5, vcc, 0, v117, vcc
	global_load_dwordx4 v[64:67], v[4:5], off offset:1792 nt
	v_lshl_add_u64 v[4:5], v[8:9], 0, s[8:9]
	global_load_dwordx4 v[72:75], v[6:7], off offset:3328
	global_load_dwordx4 v[68:71], v[4:5], off offset:16
	v_add_co_u32_e32 v4, vcc, 0x57530000, v116
	s_mov_b64 s[8:9], 0x5f51af00
	s_nop 0
	v_addc_co_u32_e32 v5, vcc, 0, v117, vcc
	global_load_dwordx4 v[52:55], v[4:5], off offset:1792 nt
	v_lshl_add_u64 v[4:5], v[8:9], 0, s[8:9]
	global_load_dwordx4 v[60:63], v[6:7], off offset:3840
	global_load_dwordx4 v[56:59], v[4:5], off offset:16
	v_add_co_u32_e32 v4, vcc, 0x57538000, v116
	s_mov_b64 s[8:9], 0x5f51b100
	s_nop 0
	v_addc_co_u32_e32 v5, vcc, 0, v117, vcc
	global_load_dwordx4 v[40:43], v[4:5], off offset:1792 nt
	v_add_co_u32_e32 v10, vcc, 0x5f51b000, v8
	v_lshl_add_u64 v[4:5], v[8:9], 0, s[8:9]
	s_nop 0
	v_addc_co_u32_e32 v11, vcc, 0, v9, vcc
	global_load_dwordx4 v[48:51], v[10:11], off offset:256
	global_load_dwordx4 v[44:47], v[4:5], off offset:16
	v_add_co_u32_e32 v4, vcc, 0x57540000, v116
	s_mov_b64 s[8:9], 0x5f51b300
	s_nop 0
	v_addc_co_u32_e32 v5, vcc, 0, v117, vcc
	global_load_dwordx4 v[28:31], v[4:5], off offset:1792 nt
	v_lshl_add_u64 v[4:5], v[8:9], 0, s[8:9]
	global_load_dwordx4 v[36:39], v[10:11], off offset:768
	global_load_dwordx4 v[32:35], v[4:5], off offset:16
	v_add_co_u32_e32 v4, vcc, 0x57548000, v116
	s_mov_b64 s[8:9], 0x5f51b500
	s_nop 0
	v_addc_co_u32_e32 v5, vcc, 0, v117, vcc
	global_load_dwordx4 v[16:19], v[4:5], off offset:1792 nt
	v_lshl_add_u64 v[4:5], v[8:9], 0, s[8:9]
	global_load_dwordx4 v[24:27], v[10:11], off offset:1280
	global_load_dwordx4 v[20:23], v[4:5], off offset:16
	v_add_co_u32_e32 v4, vcc, 0x57550000, v116
	s_mov_b64 s[8:9], 0x5f51b700
	s_nop 0
	v_addc_co_u32_e32 v5, vcc, 0, v117, vcc
	global_load_dwordx4 v[4:7], v[4:5], off offset:1792 nt
	v_lshl_add_u64 v[8:9], v[8:9], 0, s[8:9]
	global_load_dwordx4 v[12:15], v[10:11], off offset:1792
	s_nop 0
	global_load_dwordx4 v[8:11], v[8:9], off offset:16
	s_mov_b64 s[8:9], 0x40000
	v_lshl_add_u64 v[104:105], v[104:105], 0, s[10:11]
	v_lshl_add_u64 v[106:107], v[106:107], 0, s[8:9]
	v_lshl_add_u64 v[248:249], s[16:17], 0, v[106:107]
	v_add_co_u32_e32 v124, vcc, 0x57518000, v248
	v_lshl_add_u64 v[128:129], s[16:17], 0, v[104:105]
	s_nop 0
	v_addc_co_u32_e32 v125, vcc, 0, v249, vcc
	global_load_dwordx4 v[204:207], v[124:125], off offset:1792 nt
	s_mov_b64 s[8:9], 0x5f51a900
	v_add_co_u32_e32 v126, vcc, 0x5f51a000, v128
	v_lshl_add_u64 v[124:125], v[128:129], 0, s[8:9]
	s_nop 0
	v_addc_co_u32_e32 v127, vcc, 0, v129, vcc
	global_load_dwordx4 v[220:223], v[126:127], off offset:2304
	global_load_dwordx4 v[216:219], v[124:125], off offset:16
	v_add_co_u32_e32 v124, vcc, 0x57520000, v248
	s_mov_b64 s[8:9], 0x5f51ab00
	s_nop 0
	v_addc_co_u32_e32 v125, vcc, 0, v249, vcc
	global_load_dwordx4 v[196:199], v[124:125], off offset:1792 nt
	v_lshl_add_u64 v[124:125], v[128:129], 0, s[8:9]
	global_load_dwordx4 v[212:215], v[126:127], off offset:2816
	global_load_dwordx4 v[208:211], v[124:125], off offset:16
	v_add_co_u32_e32 v124, vcc, 0x57528000, v248
	s_mov_b64 s[8:9], 0x5f51ad00
	s_nop 0
	v_addc_co_u32_e32 v125, vcc, 0, v249, vcc
	global_load_dwordx4 v[184:187], v[124:125], off offset:1792 nt
	v_lshl_add_u64 v[124:125], v[128:129], 0, s[8:9]
	global_load_dwordx4 v[192:195], v[126:127], off offset:3328
	global_load_dwordx4 v[188:191], v[124:125], off offset:16
	v_add_co_u32_e32 v124, vcc, 0x57530000, v248
	s_mov_b64 s[8:9], 0x5f51af00
	s_nop 0
	v_addc_co_u32_e32 v125, vcc, 0, v249, vcc
	global_load_dwordx4 v[172:175], v[124:125], off offset:1792 nt
	v_lshl_add_u64 v[124:125], v[128:129], 0, s[8:9]
	global_load_dwordx4 v[180:183], v[126:127], off offset:3840
	global_load_dwordx4 v[176:179], v[124:125], off offset:16
	v_add_co_u32_e32 v124, vcc, 0x57538000, v248
	s_mov_b64 s[8:9], 0x5f51b100
	s_nop 0
	v_addc_co_u32_e32 v125, vcc, 0, v249, vcc
	global_load_dwordx4 v[160:163], v[124:125], off offset:1792 nt
	v_add_co_u32_e32 v130, vcc, 0x5f51b000, v128
	v_lshl_add_u64 v[124:125], v[128:129], 0, s[8:9]
	s_nop 0
	v_addc_co_u32_e32 v131, vcc, 0, v129, vcc
	global_load_dwordx4 v[168:171], v[130:131], off offset:256
	global_load_dwordx4 v[164:167], v[124:125], off offset:16
	v_add_co_u32_e32 v124, vcc, 0x57540000, v248
	s_mov_b64 s[8:9], 0x5f51b300
	s_nop 0
	v_addc_co_u32_e32 v125, vcc, 0, v249, vcc
	global_load_dwordx4 v[148:151], v[124:125], off offset:1792 nt
	v_lshl_add_u64 v[124:125], v[128:129], 0, s[8:9]
	global_load_dwordx4 v[156:159], v[130:131], off offset:768
	global_load_dwordx4 v[152:155], v[124:125], off offset:16
	v_add_co_u32_e32 v124, vcc, 0x57548000, v248
	s_mov_b64 s[8:9], 0x5f51b500
	s_nop 0
	v_addc_co_u32_e32 v125, vcc, 0, v249, vcc
	global_load_dwordx4 v[136:139], v[124:125], off offset:1792 nt
	v_lshl_add_u64 v[124:125], v[128:129], 0, s[8:9]
	global_load_dwordx4 v[144:147], v[130:131], off offset:1280
	global_load_dwordx4 v[140:143], v[124:125], off offset:16
	v_add_co_u32_e32 v124, vcc, 0x57550000, v248
	s_mov_b64 s[8:9], 0x5f51b700
	s_nop 0
	v_addc_co_u32_e32 v125, vcc, 0, v249, vcc
	global_load_dwordx4 v[124:127], v[124:125], off offset:1792 nt
	v_lshl_add_u64 v[128:129], v[128:129], 0, s[8:9]
	global_load_dwordx4 v[132:135], v[130:131], off offset:1792
	s_nop 0
	global_load_dwordx4 v[128:131], v[128:129], off offset:16
	s_mov_b64 s[8:9], 0x40000
	v_lshl_add_u64 v[104:105], v[104:105], 0, s[10:11]
	v_lshl_add_u64 v[106:107], v[106:107], 0, s[8:9]
	s_waitcnt vmcnt(24)
	s_mov_b32 s7, 0x5b519000
	v_add_co_u32_e32 v122, vcc, s7, v116
	v_cvt_pk_bf16_f32 v118, v112, v113
	v_cvt_pk_bf16_f32 v119, v114, v115
	v_cvt_pk_bf16_f32 v120, v108, v109
	v_cvt_pk_bf16_f32 v121, v110, v111
	v_addc_co_u32_e32 v123, vcc, 0, v117, vcc
	global_store_dwordx4 v[122:123], v[118:121], off offset:2048
	s_mov_b32 s7, 0x5b521000
	v_lshlrev_b32_e32 v118, 16, v80
	v_and_b32_e32 v119, 0xffff0000, v80
	v_lshlrev_b32_e32 v80, 16, v81
	v_and_b32_e32 v81, 0xffff0000, v81
	v_pk_fma_f32 v[102:103], v[114:115], v[102:103], v[80:81]
	v_lshlrev_b32_e32 v80, 16, v82
	v_and_b32_e32 v81, 0xffff0000, v82
	v_lshlrev_b32_e32 v82, 16, v83
	v_and_b32_e32 v83, 0xffff0000, v83
	v_pk_fma_f32 v[100:101], v[112:113], v[100:101], v[118:119]
	v_pk_fma_f32 v[98:99], v[110:111], v[98:99], v[82:83]
	v_pk_fma_f32 v[96:97], v[108:109], v[96:97], v[80:81]
	v_add_co_u32_e32 v108, vcc, s7, v116
	v_cvt_pk_bf16_f32 v80, v100, v101
	v_cvt_pk_bf16_f32 v81, v102, v103
	v_cvt_pk_bf16_f32 v82, v96, v97
	v_cvt_pk_bf16_f32 v83, v98, v99
	v_addc_co_u32_e32 v109, vcc, 0, v117, vcc
	global_store_dwordx4 v[108:109], v[80:83], off offset:2048
	s_mov_b32 s7, 0x5b529000
	v_lshlrev_b32_e32 v80, 16, v76
	v_and_b32_e32 v81, 0xffff0000, v76
	v_lshlrev_b32_e32 v76, 16, v77
	v_and_b32_e32 v77, 0xffff0000, v77
	v_pk_fma_f32 v[82:83], v[94:95], v[102:103], v[76:77]
	v_lshlrev_b32_e32 v76, 16, v78
	v_and_b32_e32 v77, 0xffff0000, v78
	v_lshlrev_b32_e32 v78, 16, v79
	v_and_b32_e32 v79, 0xffff0000, v79
	v_pk_fma_f32 v[80:81], v[92:93], v[100:101], v[80:81]
	v_pk_fma_f32 v[90:91], v[90:91], v[98:99], v[78:79]
	v_pk_fma_f32 v[88:89], v[88:89], v[96:97], v[76:77]
	v_add_co_u32_e32 v92, vcc, s7, v116
	v_cvt_pk_bf16_f32 v76, v80, v81
	v_cvt_pk_bf16_f32 v77, v82, v83
	v_cvt_pk_bf16_f32 v78, v88, v89
	v_cvt_pk_bf16_f32 v79, v90, v91
	v_addc_co_u32_e32 v93, vcc, 0, v117, vcc
	global_store_dwordx4 v[92:93], v[76:79], off offset:2048
	s_mov_b32 s7, 0x5b531000
	v_lshlrev_b32_e32 v76, 16, v64
	v_and_b32_e32 v77, 0xffff0000, v64
	v_lshlrev_b32_e32 v64, 16, v65
	v_and_b32_e32 v65, 0xffff0000, v65
	v_pk_fma_f32 v[74:75], v[74:75], v[82:83], v[64:65]
	v_lshlrev_b32_e32 v64, 16, v66
	v_and_b32_e32 v65, 0xffff0000, v66
	v_lshlrev_b32_e32 v66, 16, v67
	v_and_b32_e32 v67, 0xffff0000, v67
	v_pk_fma_f32 v[72:73], v[72:73], v[80:81], v[76:77]
	v_pk_fma_f32 v[70:71], v[70:71], v[90:91], v[66:67]
	v_pk_fma_f32 v[68:69], v[68:69], v[88:89], v[64:65]
	v_add_co_u32_e32 v76, vcc, s7, v116
	v_cvt_pk_bf16_f32 v64, v72, v73
	v_cvt_pk_bf16_f32 v65, v74, v75
	v_cvt_pk_bf16_f32 v66, v68, v69
	v_cvt_pk_bf16_f32 v67, v70, v71
	v_addc_co_u32_e32 v77, vcc, 0, v117, vcc
	global_store_dwordx4 v[76:77], v[64:67], off offset:2048
	s_mov_b32 s7, 0x5b539000
	s_nop 0
	v_lshlrev_b32_e32 v64, 16, v52
	v_and_b32_e32 v65, 0xffff0000, v52
	v_lshlrev_b32_e32 v52, 16, v53
	v_and_b32_e32 v53, 0xffff0000, v53
	v_pk_fma_f32 v[62:63], v[62:63], v[74:75], v[52:53]
	v_lshlrev_b32_e32 v52, 16, v54
	v_and_b32_e32 v53, 0xffff0000, v54
	v_lshlrev_b32_e32 v54, 16, v55
	v_and_b32_e32 v55, 0xffff0000, v55
	v_pk_fma_f32 v[60:61], v[60:61], v[72:73], v[64:65]
	v_pk_fma_f32 v[58:59], v[58:59], v[70:71], v[54:55]
	v_pk_fma_f32 v[56:57], v[56:57], v[68:69], v[52:53]
	v_add_co_u32_e32 v64, vcc, s7, v116
	v_cvt_pk_bf16_f32 v52, v60, v61
	v_cvt_pk_bf16_f32 v53, v62, v63
	v_cvt_pk_bf16_f32 v54, v56, v57
	v_cvt_pk_bf16_f32 v55, v58, v59
	v_addc_co_u32_e32 v65, vcc, 0, v117, vcc
	global_store_dwordx4 v[64:65], v[52:55], off offset:2048
	s_mov_b32 s7, 0x5b541000
	s_nop 0
	v_lshlrev_b32_e32 v52, 16, v40
	v_and_b32_e32 v53, 0xffff0000, v40
	v_lshlrev_b32_e32 v40, 16, v41
	v_and_b32_e32 v41, 0xffff0000, v41
	v_pk_fma_f32 v[50:51], v[50:51], v[62:63], v[40:41]
	v_lshlrev_b32_e32 v40, 16, v42
	v_and_b32_e32 v41, 0xffff0000, v42
	v_lshlrev_b32_e32 v42, 16, v43
	v_and_b32_e32 v43, 0xffff0000, v43
	v_pk_fma_f32 v[48:49], v[48:49], v[60:61], v[52:53]
	v_pk_fma_f32 v[46:47], v[46:47], v[58:59], v[42:43]
	v_pk_fma_f32 v[44:45], v[44:45], v[56:57], v[40:41]
	v_add_co_u32_e32 v52, vcc, s7, v116
	v_cvt_pk_bf16_f32 v40, v48, v49
	v_cvt_pk_bf16_f32 v41, v50, v51
	v_cvt_pk_bf16_f32 v42, v44, v45
	v_cvt_pk_bf16_f32 v43, v46, v47
	v_addc_co_u32_e32 v53, vcc, 0, v117, vcc
	global_store_dwordx4 v[52:53], v[40:43], off offset:2048
	s_mov_b32 s7, 0x5b549000
	s_nop 0
	v_lshlrev_b32_e32 v40, 16, v28
	v_and_b32_e32 v41, 0xffff0000, v28
	v_lshlrev_b32_e32 v28, 16, v29
	v_and_b32_e32 v29, 0xffff0000, v29
	v_pk_fma_f32 v[38:39], v[38:39], v[50:51], v[28:29]
	v_lshlrev_b32_e32 v28, 16, v30
	v_and_b32_e32 v29, 0xffff0000, v30
	v_lshlrev_b32_e32 v30, 16, v31
	v_and_b32_e32 v31, 0xffff0000, v31
	v_pk_fma_f32 v[36:37], v[36:37], v[48:49], v[40:41]
	v_pk_fma_f32 v[34:35], v[34:35], v[46:47], v[30:31]
	v_pk_fma_f32 v[32:33], v[32:33], v[44:45], v[28:29]
	v_add_co_u32_e32 v40, vcc, s7, v116
	v_cvt_pk_bf16_f32 v28, v36, v37
	v_cvt_pk_bf16_f32 v29, v38, v39
	v_cvt_pk_bf16_f32 v30, v32, v33
	v_cvt_pk_bf16_f32 v31, v34, v35
	v_addc_co_u32_e32 v41, vcc, 0, v117, vcc
	global_store_dwordx4 v[40:41], v[28:31], off offset:2048
	s_mov_b32 s7, 0x5b551000
	s_nop 0
	v_lshlrev_b32_e32 v28, 16, v16
	v_and_b32_e32 v29, 0xffff0000, v16
	v_lshlrev_b32_e32 v16, 16, v17
	v_and_b32_e32 v17, 0xffff0000, v17
	v_pk_fma_f32 v[26:27], v[26:27], v[38:39], v[16:17]
	v_lshlrev_b32_e32 v16, 16, v18
	v_and_b32_e32 v17, 0xffff0000, v18
	v_lshlrev_b32_e32 v18, 16, v19
	v_and_b32_e32 v19, 0xffff0000, v19
	v_pk_fma_f32 v[24:25], v[24:25], v[36:37], v[28:29]
	v_pk_fma_f32 v[22:23], v[22:23], v[34:35], v[18:19]
	v_pk_fma_f32 v[20:21], v[20:21], v[32:33], v[16:17]
	v_add_co_u32_e32 v28, vcc, s7, v116
	v_cvt_pk_bf16_f32 v16, v24, v25
	v_cvt_pk_bf16_f32 v17, v26, v27
	v_cvt_pk_bf16_f32 v18, v20, v21
	v_cvt_pk_bf16_f32 v19, v22, v23
	v_addc_co_u32_e32 v29, vcc, 0, v117, vcc
	global_store_dwordx4 v[28:29], v[16:19], off offset:2048
	s_nop 1
	v_lshlrev_b32_e32 v16, 16, v4
	v_and_b32_e32 v17, 0xffff0000, v4
	v_lshlrev_b32_e32 v4, 16, v5
	v_and_b32_e32 v5, 0xffff0000, v5
	v_pk_fma_f32 v[114:115], v[14:15], v[26:27], v[4:5]
	v_lshlrev_b32_e32 v4, 16, v6
	v_and_b32_e32 v5, 0xffff0000, v6
	v_lshlrev_b32_e32 v6, 16, v7
	v_and_b32_e32 v7, 0xffff0000, v7
	v_pk_fma_f32 v[112:113], v[12:13], v[24:25], v[16:17]
	v_pk_fma_f32 v[110:111], v[10:11], v[22:23], v[6:7]
	v_pk_fma_f32 v[108:109], v[8:9], v[20:21], v[4:5]
	v_lshl_add_u64 v[116:117], s[16:17], 0, v[106:107]
	v_add_co_u32_e32 v4, vcc, 0x57518000, v116
	v_lshl_add_u64 v[8:9], s[16:17], 0, v[104:105]
	s_nop 0
	v_addc_co_u32_e32 v5, vcc, 0, v117, vcc
	global_load_dwordx4 v[80:83], v[4:5], off offset:1792 nt
	s_mov_b64 s[8:9], 0x5f51a900
	v_add_co_u32_e32 v6, vcc, 0x5f51a000, v8
	v_lshl_add_u64 v[4:5], v[8:9], 0, s[8:9]
	s_nop 0
	v_addc_co_u32_e32 v7, vcc, 0, v9, vcc
	global_load_dwordx4 v[100:103], v[6:7], off offset:2304
	global_load_dwordx4 v[96:99], v[4:5], off offset:16
	v_add_co_u32_e32 v4, vcc, 0x57520000, v116
	s_mov_b64 s[8:9], 0x5f51ab00
	s_nop 0
	v_addc_co_u32_e32 v5, vcc, 0, v117, vcc
	global_load_dwordx4 v[76:79], v[4:5], off offset:1792 nt
	v_lshl_add_u64 v[4:5], v[8:9], 0, s[8:9]
	global_load_dwordx4 v[92:95], v[6:7], off offset:2816
	global_load_dwordx4 v[88:91], v[4:5], off offset:16
	v_add_co_u32_e32 v4, vcc, 0x57528000, v116
	s_mov_b64 s[8:9], 0x5f51ad00
	s_nop 0
	v_addc_co_u32_e32 v5, vcc, 0, v117, vcc
	global_load_dwordx4 v[64:67], v[4:5], off offset:1792 nt
	v_lshl_add_u64 v[4:5], v[8:9], 0, s[8:9]
	global_load_dwordx4 v[72:75], v[6:7], off offset:3328
	global_load_dwordx4 v[68:71], v[4:5], off offset:16
	v_add_co_u32_e32 v4, vcc, 0x57530000, v116
	s_mov_b64 s[8:9], 0x5f51af00
	s_nop 0
	v_addc_co_u32_e32 v5, vcc, 0, v117, vcc
	global_load_dwordx4 v[52:55], v[4:5], off offset:1792 nt
	v_lshl_add_u64 v[4:5], v[8:9], 0, s[8:9]
	global_load_dwordx4 v[60:63], v[6:7], off offset:3840
	global_load_dwordx4 v[56:59], v[4:5], off offset:16
	v_add_co_u32_e32 v4, vcc, 0x57538000, v116
	s_mov_b64 s[8:9], 0x5f51b100
	s_nop 0
	v_addc_co_u32_e32 v5, vcc, 0, v117, vcc
	global_load_dwordx4 v[40:43], v[4:5], off offset:1792 nt
	v_add_co_u32_e32 v10, vcc, 0x5f51b000, v8
	v_lshl_add_u64 v[4:5], v[8:9], 0, s[8:9]
	s_nop 0
	v_addc_co_u32_e32 v11, vcc, 0, v9, vcc
	global_load_dwordx4 v[48:51], v[10:11], off offset:256
	global_load_dwordx4 v[44:47], v[4:5], off offset:16
	v_add_co_u32_e32 v4, vcc, 0x57540000, v116
	s_mov_b64 s[8:9], 0x5f51b300
	s_nop 0
	v_addc_co_u32_e32 v5, vcc, 0, v117, vcc
	global_load_dwordx4 v[28:31], v[4:5], off offset:1792 nt
	v_lshl_add_u64 v[4:5], v[8:9], 0, s[8:9]
	global_load_dwordx4 v[36:39], v[10:11], off offset:768
	global_load_dwordx4 v[32:35], v[4:5], off offset:16
	v_add_co_u32_e32 v4, vcc, 0x57548000, v116
	s_mov_b64 s[8:9], 0x5f51b500
	s_nop 0
	v_addc_co_u32_e32 v5, vcc, 0, v117, vcc
	global_load_dwordx4 v[16:19], v[4:5], off offset:1792 nt
	v_lshl_add_u64 v[4:5], v[8:9], 0, s[8:9]
	global_load_dwordx4 v[24:27], v[10:11], off offset:1280
	global_load_dwordx4 v[20:23], v[4:5], off offset:16
	v_add_co_u32_e32 v4, vcc, 0x57550000, v116
	s_mov_b64 s[8:9], 0x5f51b700
	s_nop 0
	v_addc_co_u32_e32 v5, vcc, 0, v117, vcc
	global_load_dwordx4 v[4:7], v[4:5], off offset:1792 nt
	v_lshl_add_u64 v[8:9], v[8:9], 0, s[8:9]
	global_load_dwordx4 v[12:15], v[10:11], off offset:1792
	s_nop 0
	global_load_dwordx4 v[8:11], v[8:9], off offset:16
	s_mov_b64 s[8:9], 0x40000
	v_lshl_add_u64 v[104:105], v[104:105], 0, s[10:11]
	v_lshl_add_u64 v[106:107], v[106:107], 0, s[8:9]
	s_waitcnt vmcnt(32)
	s_mov_b32 s7, 0x5b519000
	v_add_co_u32_e32 v122, vcc, s7, v248
	v_cvt_pk_bf16_f32 v118, v112, v113
	v_cvt_pk_bf16_f32 v119, v114, v115
	v_cvt_pk_bf16_f32 v120, v108, v109
	v_cvt_pk_bf16_f32 v121, v110, v111
	v_addc_co_u32_e32 v123, vcc, 0, v249, vcc
	global_store_dwordx4 v[122:123], v[118:121], off offset:2048
	s_mov_b32 s7, 0x5b521000
	v_lshlrev_b32_e32 v118, 16, v204
	v_and_b32_e32 v119, 0xffff0000, v204
	v_lshlrev_b32_e32 v204, 16, v205
	v_and_b32_e32 v205, 0xffff0000, v205
	v_pk_fma_f32 v[222:223], v[114:115], v[222:223], v[204:205]
	v_lshlrev_b32_e32 v204, 16, v206
	v_and_b32_e32 v205, 0xffff0000, v206
	v_lshlrev_b32_e32 v206, 16, v207
	v_and_b32_e32 v207, 0xffff0000, v207
	v_pk_fma_f32 v[220:221], v[112:113], v[220:221], v[118:119]
	v_pk_fma_f32 v[218:219], v[110:111], v[218:219], v[206:207]
	v_pk_fma_f32 v[216:217], v[108:109], v[216:217], v[204:205]
	v_add_co_u32_e32 v108, vcc, s7, v248
	v_cvt_pk_bf16_f32 v204, v220, v221
	v_cvt_pk_bf16_f32 v205, v222, v223
	v_cvt_pk_bf16_f32 v206, v216, v217
	v_cvt_pk_bf16_f32 v207, v218, v219
	v_addc_co_u32_e32 v109, vcc, 0, v249, vcc
	global_store_dwordx4 v[108:109], v[204:207], off offset:2048
	s_mov_b32 s7, 0x5b529000
	v_lshlrev_b32_e32 v204, 16, v196
	v_and_b32_e32 v205, 0xffff0000, v196
	v_lshlrev_b32_e32 v196, 16, v197
	v_and_b32_e32 v197, 0xffff0000, v197
	v_pk_fma_f32 v[206:207], v[214:215], v[222:223], v[196:197]
	v_lshlrev_b32_e32 v196, 16, v198
	v_and_b32_e32 v197, 0xffff0000, v198
	v_lshlrev_b32_e32 v198, 16, v199
	v_and_b32_e32 v199, 0xffff0000, v199
	v_pk_fma_f32 v[204:205], v[212:213], v[220:221], v[204:205]
	v_pk_fma_f32 v[210:211], v[210:211], v[218:219], v[198:199]
	v_pk_fma_f32 v[208:209], v[208:209], v[216:217], v[196:197]
	v_add_co_u32_e32 v212, vcc, s7, v248
	v_cvt_pk_bf16_f32 v196, v204, v205
	v_cvt_pk_bf16_f32 v197, v206, v207
	v_cvt_pk_bf16_f32 v198, v208, v209
	v_cvt_pk_bf16_f32 v199, v210, v211
	v_addc_co_u32_e32 v213, vcc, 0, v249, vcc
	global_store_dwordx4 v[212:213], v[196:199], off offset:2048
	s_mov_b32 s7, 0x5b531000
	v_lshlrev_b32_e32 v196, 16, v184
	v_and_b32_e32 v197, 0xffff0000, v184
	v_lshlrev_b32_e32 v184, 16, v185
	v_and_b32_e32 v185, 0xffff0000, v185
	v_pk_fma_f32 v[194:195], v[194:195], v[206:207], v[184:185]
	v_lshlrev_b32_e32 v184, 16, v186
	v_and_b32_e32 v185, 0xffff0000, v186
	v_lshlrev_b32_e32 v186, 16, v187
	v_and_b32_e32 v187, 0xffff0000, v187
	v_pk_fma_f32 v[192:193], v[192:193], v[204:205], v[196:197]
	v_pk_fma_f32 v[190:191], v[190:191], v[210:211], v[186:187]
	v_pk_fma_f32 v[188:189], v[188:189], v[208:209], v[184:185]
	v_add_co_u32_e32 v196, vcc, s7, v248
	v_cvt_pk_bf16_f32 v184, v192, v193
	v_cvt_pk_bf16_f32 v185, v194, v195
	v_cvt_pk_bf16_f32 v186, v188, v189
	v_cvt_pk_bf16_f32 v187, v190, v191
	v_addc_co_u32_e32 v197, vcc, 0, v249, vcc
	global_store_dwordx4 v[196:197], v[184:187], off offset:2048
	s_mov_b32 s7, 0x5b539000
	s_nop 0
	v_lshlrev_b32_e32 v184, 16, v172
	v_and_b32_e32 v185, 0xffff0000, v172
	v_lshlrev_b32_e32 v172, 16, v173
	v_and_b32_e32 v173, 0xffff0000, v173
	v_pk_fma_f32 v[182:183], v[182:183], v[194:195], v[172:173]
	v_lshlrev_b32_e32 v172, 16, v174
	v_and_b32_e32 v173, 0xffff0000, v174
	v_lshlrev_b32_e32 v174, 16, v175
	v_and_b32_e32 v175, 0xffff0000, v175
	v_pk_fma_f32 v[180:181], v[180:181], v[192:193], v[184:185]
	v_pk_fma_f32 v[178:179], v[178:179], v[190:191], v[174:175]
	v_pk_fma_f32 v[176:177], v[176:177], v[188:189], v[172:173]
	v_add_co_u32_e32 v184, vcc, s7, v248
	v_cvt_pk_bf16_f32 v172, v180, v181
	v_cvt_pk_bf16_f32 v173, v182, v183
	v_cvt_pk_bf16_f32 v174, v176, v177
	v_cvt_pk_bf16_f32 v175, v178, v179
	v_addc_co_u32_e32 v185, vcc, 0, v249, vcc
	global_store_dwordx4 v[184:185], v[172:175], off offset:2048
	s_mov_b32 s7, 0x5b541000
	s_nop 0
	v_lshlrev_b32_e32 v172, 16, v160
	v_and_b32_e32 v173, 0xffff0000, v160
	v_lshlrev_b32_e32 v160, 16, v161
	v_and_b32_e32 v161, 0xffff0000, v161
	v_pk_fma_f32 v[170:171], v[170:171], v[182:183], v[160:161]
	v_lshlrev_b32_e32 v160, 16, v162
	v_and_b32_e32 v161, 0xffff0000, v162
	v_lshlrev_b32_e32 v162, 16, v163
	v_and_b32_e32 v163, 0xffff0000, v163
	v_pk_fma_f32 v[168:169], v[168:169], v[180:181], v[172:173]
	v_pk_fma_f32 v[166:167], v[166:167], v[178:179], v[162:163]
	v_pk_fma_f32 v[164:165], v[164:165], v[176:177], v[160:161]
	v_add_co_u32_e32 v172, vcc, s7, v248
	v_cvt_pk_bf16_f32 v160, v168, v169
	v_cvt_pk_bf16_f32 v161, v170, v171
	v_cvt_pk_bf16_f32 v162, v164, v165
	v_cvt_pk_bf16_f32 v163, v166, v167
	v_addc_co_u32_e32 v173, vcc, 0, v249, vcc
	global_store_dwordx4 v[172:173], v[160:163], off offset:2048
	s_mov_b32 s7, 0x5b549000
	s_nop 0
	v_lshlrev_b32_e32 v160, 16, v148
	v_and_b32_e32 v161, 0xffff0000, v148
	v_lshlrev_b32_e32 v148, 16, v149
	v_and_b32_e32 v149, 0xffff0000, v149
	v_pk_fma_f32 v[158:159], v[158:159], v[170:171], v[148:149]
	v_lshlrev_b32_e32 v148, 16, v150
	v_and_b32_e32 v149, 0xffff0000, v150
	v_lshlrev_b32_e32 v150, 16, v151
	v_and_b32_e32 v151, 0xffff0000, v151
	v_pk_fma_f32 v[156:157], v[156:157], v[168:169], v[160:161]
	v_pk_fma_f32 v[154:155], v[154:155], v[166:167], v[150:151]
	v_pk_fma_f32 v[152:153], v[152:153], v[164:165], v[148:149]
	v_add_co_u32_e32 v160, vcc, s7, v248
	v_cvt_pk_bf16_f32 v148, v156, v157
	v_cvt_pk_bf16_f32 v149, v158, v159
	v_cvt_pk_bf16_f32 v150, v152, v153
	v_cvt_pk_bf16_f32 v151, v154, v155
	v_addc_co_u32_e32 v161, vcc, 0, v249, vcc
	global_store_dwordx4 v[160:161], v[148:151], off offset:2048
	s_mov_b32 s7, 0x5b551000
	s_nop 0
	v_lshlrev_b32_e32 v148, 16, v136
	v_and_b32_e32 v149, 0xffff0000, v136
	v_lshlrev_b32_e32 v136, 16, v137
	v_and_b32_e32 v137, 0xffff0000, v137
	v_pk_fma_f32 v[146:147], v[146:147], v[158:159], v[136:137]
	v_lshlrev_b32_e32 v136, 16, v138
	v_and_b32_e32 v137, 0xffff0000, v138
	v_lshlrev_b32_e32 v138, 16, v139
	v_and_b32_e32 v139, 0xffff0000, v139
	v_pk_fma_f32 v[144:145], v[144:145], v[156:157], v[148:149]
	v_pk_fma_f32 v[142:143], v[142:143], v[154:155], v[138:139]
	v_pk_fma_f32 v[140:141], v[140:141], v[152:153], v[136:137]
	v_add_co_u32_e32 v148, vcc, s7, v248
	v_cvt_pk_bf16_f32 v136, v144, v145
	v_cvt_pk_bf16_f32 v137, v146, v147
	v_cvt_pk_bf16_f32 v138, v140, v141
	v_cvt_pk_bf16_f32 v139, v142, v143
	v_addc_co_u32_e32 v149, vcc, 0, v249, vcc
	global_store_dwordx4 v[148:149], v[136:139], off offset:2048
	s_nop 1
	v_lshlrev_b32_e32 v136, 16, v124
	v_and_b32_e32 v137, 0xffff0000, v124
	v_lshlrev_b32_e32 v124, 16, v125
	v_and_b32_e32 v125, 0xffff0000, v125
	v_pk_fma_f32 v[114:115], v[134:135], v[146:147], v[124:125]
	v_lshlrev_b32_e32 v124, 16, v126
	v_and_b32_e32 v125, 0xffff0000, v126
	v_lshlrev_b32_e32 v126, 16, v127
	v_and_b32_e32 v127, 0xffff0000, v127
	v_pk_fma_f32 v[112:113], v[132:133], v[144:145], v[136:137]
	v_pk_fma_f32 v[110:111], v[130:131], v[142:143], v[126:127]
	v_pk_fma_f32 v[108:109], v[128:129], v[140:141], v[124:125]
	v_lshl_add_u64 v[248:249], s[16:17], 0, v[106:107]
	v_add_co_u32_e32 v124, vcc, 0x57518000, v248
	v_lshl_add_u64 v[128:129], s[16:17], 0, v[104:105]
	s_nop 0
	v_addc_co_u32_e32 v125, vcc, 0, v249, vcc
	global_load_dwordx4 v[204:207], v[124:125], off offset:1792 nt
	s_mov_b64 s[8:9], 0x5f51a900
	v_add_co_u32_e32 v126, vcc, 0x5f51a000, v128
	v_lshl_add_u64 v[124:125], v[128:129], 0, s[8:9]
	s_nop 0
	v_addc_co_u32_e32 v127, vcc, 0, v129, vcc
	global_load_dwordx4 v[220:223], v[126:127], off offset:2304
	global_load_dwordx4 v[216:219], v[124:125], off offset:16
	v_add_co_u32_e32 v124, vcc, 0x57520000, v248
	s_mov_b64 s[8:9], 0x5f51ab00
	s_nop 0
	v_addc_co_u32_e32 v125, vcc, 0, v249, vcc
	global_load_dwordx4 v[196:199], v[124:125], off offset:1792 nt
	v_lshl_add_u64 v[124:125], v[128:129], 0, s[8:9]
	global_load_dwordx4 v[212:215], v[126:127], off offset:2816
	global_load_dwordx4 v[208:211], v[124:125], off offset:16
	v_add_co_u32_e32 v124, vcc, 0x57528000, v248
	s_mov_b64 s[8:9], 0x5f51ad00
	s_nop 0
	v_addc_co_u32_e32 v125, vcc, 0, v249, vcc
	global_load_dwordx4 v[184:187], v[124:125], off offset:1792 nt
	v_lshl_add_u64 v[124:125], v[128:129], 0, s[8:9]
	global_load_dwordx4 v[192:195], v[126:127], off offset:3328
	global_load_dwordx4 v[188:191], v[124:125], off offset:16
	v_add_co_u32_e32 v124, vcc, 0x57530000, v248
	s_mov_b64 s[8:9], 0x5f51af00
	s_nop 0
	v_addc_co_u32_e32 v125, vcc, 0, v249, vcc
	global_load_dwordx4 v[172:175], v[124:125], off offset:1792 nt
	v_lshl_add_u64 v[124:125], v[128:129], 0, s[8:9]
	global_load_dwordx4 v[180:183], v[126:127], off offset:3840
	global_load_dwordx4 v[176:179], v[124:125], off offset:16
	v_add_co_u32_e32 v124, vcc, 0x57538000, v248
	s_mov_b64 s[8:9], 0x5f51b100
	s_nop 0
	v_addc_co_u32_e32 v125, vcc, 0, v249, vcc
	global_load_dwordx4 v[160:163], v[124:125], off offset:1792 nt
	v_add_co_u32_e32 v130, vcc, 0x5f51b000, v128
	v_lshl_add_u64 v[124:125], v[128:129], 0, s[8:9]
	s_nop 0
	v_addc_co_u32_e32 v131, vcc, 0, v129, vcc
	global_load_dwordx4 v[168:171], v[130:131], off offset:256
	global_load_dwordx4 v[164:167], v[124:125], off offset:16
	v_add_co_u32_e32 v124, vcc, 0x57540000, v248
	s_mov_b64 s[8:9], 0x5f51b300
	s_nop 0
	v_addc_co_u32_e32 v125, vcc, 0, v249, vcc
	global_load_dwordx4 v[148:151], v[124:125], off offset:1792 nt
	v_lshl_add_u64 v[124:125], v[128:129], 0, s[8:9]
	global_load_dwordx4 v[156:159], v[130:131], off offset:768
	global_load_dwordx4 v[152:155], v[124:125], off offset:16
	v_add_co_u32_e32 v124, vcc, 0x57548000, v248
	s_mov_b64 s[8:9], 0x5f51b500
	s_nop 0
	v_addc_co_u32_e32 v125, vcc, 0, v249, vcc
	global_load_dwordx4 v[136:139], v[124:125], off offset:1792 nt
	v_lshl_add_u64 v[124:125], v[128:129], 0, s[8:9]
	global_load_dwordx4 v[144:147], v[130:131], off offset:1280
	global_load_dwordx4 v[140:143], v[124:125], off offset:16
	v_add_co_u32_e32 v124, vcc, 0x57550000, v248
	s_mov_b64 s[8:9], 0x5f51b700
	s_nop 0
	v_addc_co_u32_e32 v125, vcc, 0, v249, vcc
	global_load_dwordx4 v[124:127], v[124:125], off offset:1792 nt
	v_lshl_add_u64 v[128:129], v[128:129], 0, s[8:9]
	global_load_dwordx4 v[132:135], v[130:131], off offset:1792
	s_nop 0
	global_load_dwordx4 v[128:131], v[128:129], off offset:16
	s_mov_b64 s[8:9], 0x40000
	v_lshl_add_u64 v[104:105], v[104:105], 0, s[10:11]
	v_lshl_add_u64 v[106:107], v[106:107], 0, s[8:9]
	s_waitcnt vmcnt(32)
	s_mov_b32 s7, 0x5b519000
	v_add_co_u32_e32 v122, vcc, s7, v116
	v_cvt_pk_bf16_f32 v118, v112, v113
	v_cvt_pk_bf16_f32 v119, v114, v115
	v_cvt_pk_bf16_f32 v120, v108, v109
	v_cvt_pk_bf16_f32 v121, v110, v111
	v_addc_co_u32_e32 v123, vcc, 0, v117, vcc
	global_store_dwordx4 v[122:123], v[118:121], off offset:2048
	s_mov_b32 s7, 0x5b521000
	v_lshlrev_b32_e32 v118, 16, v80
	v_and_b32_e32 v119, 0xffff0000, v80
	v_lshlrev_b32_e32 v80, 16, v81
	v_and_b32_e32 v81, 0xffff0000, v81
	v_pk_fma_f32 v[102:103], v[114:115], v[102:103], v[80:81]
	v_lshlrev_b32_e32 v80, 16, v82
	v_and_b32_e32 v81, 0xffff0000, v82
	v_lshlrev_b32_e32 v82, 16, v83
	v_and_b32_e32 v83, 0xffff0000, v83
	v_pk_fma_f32 v[100:101], v[112:113], v[100:101], v[118:119]
	v_pk_fma_f32 v[98:99], v[110:111], v[98:99], v[82:83]
	v_pk_fma_f32 v[96:97], v[108:109], v[96:97], v[80:81]
	v_add_co_u32_e32 v108, vcc, s7, v116
	v_cvt_pk_bf16_f32 v80, v100, v101
	v_cvt_pk_bf16_f32 v81, v102, v103
	v_cvt_pk_bf16_f32 v82, v96, v97
	v_cvt_pk_bf16_f32 v83, v98, v99
	v_addc_co_u32_e32 v109, vcc, 0, v117, vcc
	global_store_dwordx4 v[108:109], v[80:83], off offset:2048
	s_mov_b32 s7, 0x5b529000
	v_lshlrev_b32_e32 v80, 16, v76
	v_and_b32_e32 v81, 0xffff0000, v76
	v_lshlrev_b32_e32 v76, 16, v77
	v_and_b32_e32 v77, 0xffff0000, v77
	v_pk_fma_f32 v[82:83], v[94:95], v[102:103], v[76:77]
	v_lshlrev_b32_e32 v76, 16, v78
	v_and_b32_e32 v77, 0xffff0000, v78
	v_lshlrev_b32_e32 v78, 16, v79
	v_and_b32_e32 v79, 0xffff0000, v79
	v_pk_fma_f32 v[80:81], v[92:93], v[100:101], v[80:81]
	v_pk_fma_f32 v[90:91], v[90:91], v[98:99], v[78:79]
	v_pk_fma_f32 v[88:89], v[88:89], v[96:97], v[76:77]
	v_add_co_u32_e32 v92, vcc, s7, v116
	v_cvt_pk_bf16_f32 v76, v80, v81
	v_cvt_pk_bf16_f32 v77, v82, v83
	v_cvt_pk_bf16_f32 v78, v88, v89
	v_cvt_pk_bf16_f32 v79, v90, v91
	v_addc_co_u32_e32 v93, vcc, 0, v117, vcc
	global_store_dwordx4 v[92:93], v[76:79], off offset:2048
	s_mov_b32 s7, 0x5b531000
	v_lshlrev_b32_e32 v76, 16, v64
	v_and_b32_e32 v77, 0xffff0000, v64
	v_lshlrev_b32_e32 v64, 16, v65
	v_and_b32_e32 v65, 0xffff0000, v65
	v_pk_fma_f32 v[74:75], v[74:75], v[82:83], v[64:65]
	v_lshlrev_b32_e32 v64, 16, v66
	v_and_b32_e32 v65, 0xffff0000, v66
	v_lshlrev_b32_e32 v66, 16, v67
	v_and_b32_e32 v67, 0xffff0000, v67
	v_pk_fma_f32 v[72:73], v[72:73], v[80:81], v[76:77]
	v_pk_fma_f32 v[70:71], v[70:71], v[90:91], v[66:67]
	v_pk_fma_f32 v[68:69], v[68:69], v[88:89], v[64:65]
	v_add_co_u32_e32 v76, vcc, s7, v116
	v_cvt_pk_bf16_f32 v64, v72, v73
	v_cvt_pk_bf16_f32 v65, v74, v75
	v_cvt_pk_bf16_f32 v66, v68, v69
	v_cvt_pk_bf16_f32 v67, v70, v71
	v_addc_co_u32_e32 v77, vcc, 0, v117, vcc
	global_store_dwordx4 v[76:77], v[64:67], off offset:2048
	s_mov_b32 s7, 0x5b539000
	s_nop 0
	v_lshlrev_b32_e32 v64, 16, v52
	v_and_b32_e32 v65, 0xffff0000, v52
	v_lshlrev_b32_e32 v52, 16, v53
	v_and_b32_e32 v53, 0xffff0000, v53
	v_pk_fma_f32 v[62:63], v[62:63], v[74:75], v[52:53]
	v_lshlrev_b32_e32 v52, 16, v54
	v_and_b32_e32 v53, 0xffff0000, v54
	v_lshlrev_b32_e32 v54, 16, v55
	v_and_b32_e32 v55, 0xffff0000, v55
	v_pk_fma_f32 v[60:61], v[60:61], v[72:73], v[64:65]
	v_pk_fma_f32 v[58:59], v[58:59], v[70:71], v[54:55]
	v_pk_fma_f32 v[56:57], v[56:57], v[68:69], v[52:53]
	v_add_co_u32_e32 v64, vcc, s7, v116
	v_cvt_pk_bf16_f32 v52, v60, v61
	v_cvt_pk_bf16_f32 v53, v62, v63
	v_cvt_pk_bf16_f32 v54, v56, v57
	v_cvt_pk_bf16_f32 v55, v58, v59
	v_addc_co_u32_e32 v65, vcc, 0, v117, vcc
	global_store_dwordx4 v[64:65], v[52:55], off offset:2048
	s_mov_b32 s7, 0x5b541000
	s_nop 0
	v_lshlrev_b32_e32 v52, 16, v40
	v_and_b32_e32 v53, 0xffff0000, v40
	v_lshlrev_b32_e32 v40, 16, v41
	v_and_b32_e32 v41, 0xffff0000, v41
	v_pk_fma_f32 v[50:51], v[50:51], v[62:63], v[40:41]
	v_lshlrev_b32_e32 v40, 16, v42
	v_and_b32_e32 v41, 0xffff0000, v42
	v_lshlrev_b32_e32 v42, 16, v43
	v_and_b32_e32 v43, 0xffff0000, v43
	v_pk_fma_f32 v[48:49], v[48:49], v[60:61], v[52:53]
	v_pk_fma_f32 v[46:47], v[46:47], v[58:59], v[42:43]
	v_pk_fma_f32 v[44:45], v[44:45], v[56:57], v[40:41]
	v_add_co_u32_e32 v52, vcc, s7, v116
	v_cvt_pk_bf16_f32 v40, v48, v49
	v_cvt_pk_bf16_f32 v41, v50, v51
	v_cvt_pk_bf16_f32 v42, v44, v45
	v_cvt_pk_bf16_f32 v43, v46, v47
	v_addc_co_u32_e32 v53, vcc, 0, v117, vcc
	global_store_dwordx4 v[52:53], v[40:43], off offset:2048
	s_mov_b32 s7, 0x5b549000
	s_nop 0
	v_lshlrev_b32_e32 v40, 16, v28
	v_and_b32_e32 v41, 0xffff0000, v28
	v_lshlrev_b32_e32 v28, 16, v29
	v_and_b32_e32 v29, 0xffff0000, v29
	v_pk_fma_f32 v[38:39], v[38:39], v[50:51], v[28:29]
	v_lshlrev_b32_e32 v28, 16, v30
	v_and_b32_e32 v29, 0xffff0000, v30
	v_lshlrev_b32_e32 v30, 16, v31
	v_and_b32_e32 v31, 0xffff0000, v31
	v_pk_fma_f32 v[36:37], v[36:37], v[48:49], v[40:41]
	v_pk_fma_f32 v[34:35], v[34:35], v[46:47], v[30:31]
	v_pk_fma_f32 v[32:33], v[32:33], v[44:45], v[28:29]
	v_add_co_u32_e32 v40, vcc, s7, v116
	v_cvt_pk_bf16_f32 v28, v36, v37
	v_cvt_pk_bf16_f32 v29, v38, v39
	v_cvt_pk_bf16_f32 v30, v32, v33
	v_cvt_pk_bf16_f32 v31, v34, v35
	v_addc_co_u32_e32 v41, vcc, 0, v117, vcc
	global_store_dwordx4 v[40:41], v[28:31], off offset:2048
	s_mov_b32 s7, 0x5b551000
	s_nop 0
	v_lshlrev_b32_e32 v28, 16, v16
	v_and_b32_e32 v29, 0xffff0000, v16
	v_lshlrev_b32_e32 v16, 16, v17
	v_and_b32_e32 v17, 0xffff0000, v17
	v_pk_fma_f32 v[26:27], v[26:27], v[38:39], v[16:17]
	v_lshlrev_b32_e32 v16, 16, v18
	v_and_b32_e32 v17, 0xffff0000, v18
	v_lshlrev_b32_e32 v18, 16, v19
	v_and_b32_e32 v19, 0xffff0000, v19
	v_pk_fma_f32 v[24:25], v[24:25], v[36:37], v[28:29]
	v_pk_fma_f32 v[22:23], v[22:23], v[34:35], v[18:19]
	v_pk_fma_f32 v[20:21], v[20:21], v[32:33], v[16:17]
	v_add_co_u32_e32 v28, vcc, s7, v116
	v_cvt_pk_bf16_f32 v16, v24, v25
	v_cvt_pk_bf16_f32 v17, v26, v27
	v_cvt_pk_bf16_f32 v18, v20, v21
	v_cvt_pk_bf16_f32 v19, v22, v23
	v_addc_co_u32_e32 v29, vcc, 0, v117, vcc
	global_store_dwordx4 v[28:29], v[16:19], off offset:2048
	s_nop 1
	v_lshlrev_b32_e32 v16, 16, v4
	v_and_b32_e32 v17, 0xffff0000, v4
	v_lshlrev_b32_e32 v4, 16, v5
	v_and_b32_e32 v5, 0xffff0000, v5
	v_pk_fma_f32 v[114:115], v[14:15], v[26:27], v[4:5]
	v_lshlrev_b32_e32 v4, 16, v6
	v_and_b32_e32 v5, 0xffff0000, v6
	v_lshlrev_b32_e32 v6, 16, v7
	v_and_b32_e32 v7, 0xffff0000, v7
	v_pk_fma_f32 v[112:113], v[12:13], v[24:25], v[16:17]
	v_pk_fma_f32 v[110:111], v[10:11], v[22:23], v[6:7]
	v_pk_fma_f32 v[108:109], v[8:9], v[20:21], v[4:5]
	s_waitcnt vmcnt(8)
	s_mov_b32 s7, 0x5b519000
	v_add_co_u32_e32 v122, vcc, s7, v248
	v_cvt_pk_bf16_f32 v118, v112, v113
	v_cvt_pk_bf16_f32 v119, v114, v115
	v_cvt_pk_bf16_f32 v120, v108, v109
	v_cvt_pk_bf16_f32 v121, v110, v111
	v_addc_co_u32_e32 v123, vcc, 0, v249, vcc
	global_store_dwordx4 v[122:123], v[118:121], off offset:2048
	s_mov_b32 s7, 0x5b521000
	v_lshlrev_b32_e32 v118, 16, v204
	v_and_b32_e32 v119, 0xffff0000, v204
	v_lshlrev_b32_e32 v204, 16, v205
	v_and_b32_e32 v205, 0xffff0000, v205
	v_pk_fma_f32 v[222:223], v[114:115], v[222:223], v[204:205]
	v_lshlrev_b32_e32 v204, 16, v206
	v_and_b32_e32 v205, 0xffff0000, v206
	v_lshlrev_b32_e32 v206, 16, v207
	v_and_b32_e32 v207, 0xffff0000, v207
	v_pk_fma_f32 v[220:221], v[112:113], v[220:221], v[118:119]
	v_pk_fma_f32 v[218:219], v[110:111], v[218:219], v[206:207]
	v_pk_fma_f32 v[216:217], v[108:109], v[216:217], v[204:205]
	v_add_co_u32_e32 v108, vcc, s7, v248
	v_cvt_pk_bf16_f32 v204, v220, v221
	v_cvt_pk_bf16_f32 v205, v222, v223
	v_cvt_pk_bf16_f32 v206, v216, v217
	v_cvt_pk_bf16_f32 v207, v218, v219
	v_addc_co_u32_e32 v109, vcc, 0, v249, vcc
	global_store_dwordx4 v[108:109], v[204:207], off offset:2048
	s_mov_b32 s7, 0x5b529000
	v_lshlrev_b32_e32 v204, 16, v196
	v_and_b32_e32 v205, 0xffff0000, v196
	v_lshlrev_b32_e32 v196, 16, v197
	v_and_b32_e32 v197, 0xffff0000, v197
	v_pk_fma_f32 v[206:207], v[214:215], v[222:223], v[196:197]
	v_lshlrev_b32_e32 v196, 16, v198
	v_and_b32_e32 v197, 0xffff0000, v198
	v_lshlrev_b32_e32 v198, 16, v199
	v_and_b32_e32 v199, 0xffff0000, v199
	v_pk_fma_f32 v[204:205], v[212:213], v[220:221], v[204:205]
	v_pk_fma_f32 v[210:211], v[210:211], v[218:219], v[198:199]
	v_pk_fma_f32 v[208:209], v[208:209], v[216:217], v[196:197]
	v_add_co_u32_e32 v212, vcc, s7, v248
	v_cvt_pk_bf16_f32 v196, v204, v205
	v_cvt_pk_bf16_f32 v197, v206, v207
	v_cvt_pk_bf16_f32 v198, v208, v209
	v_cvt_pk_bf16_f32 v199, v210, v211
	v_addc_co_u32_e32 v213, vcc, 0, v249, vcc
	global_store_dwordx4 v[212:213], v[196:199], off offset:2048
	s_mov_b32 s7, 0x5b531000
	v_lshlrev_b32_e32 v196, 16, v184
	v_and_b32_e32 v197, 0xffff0000, v184
	v_lshlrev_b32_e32 v184, 16, v185
	v_and_b32_e32 v185, 0xffff0000, v185
	v_pk_fma_f32 v[194:195], v[194:195], v[206:207], v[184:185]
	v_lshlrev_b32_e32 v184, 16, v186
	v_and_b32_e32 v185, 0xffff0000, v186
	v_lshlrev_b32_e32 v186, 16, v187
	v_and_b32_e32 v187, 0xffff0000, v187
	v_pk_fma_f32 v[192:193], v[192:193], v[204:205], v[196:197]
	v_pk_fma_f32 v[190:191], v[190:191], v[210:211], v[186:187]
	v_pk_fma_f32 v[188:189], v[188:189], v[208:209], v[184:185]
	v_add_co_u32_e32 v196, vcc, s7, v248
	v_cvt_pk_bf16_f32 v184, v192, v193
	v_cvt_pk_bf16_f32 v185, v194, v195
	v_cvt_pk_bf16_f32 v186, v188, v189
	v_cvt_pk_bf16_f32 v187, v190, v191
	v_addc_co_u32_e32 v197, vcc, 0, v249, vcc
	global_store_dwordx4 v[196:197], v[184:187], off offset:2048
	s_mov_b32 s7, 0x5b539000
	s_nop 0
	v_lshlrev_b32_e32 v184, 16, v172
	v_and_b32_e32 v185, 0xffff0000, v172
	v_lshlrev_b32_e32 v172, 16, v173
	v_and_b32_e32 v173, 0xffff0000, v173
	v_pk_fma_f32 v[182:183], v[182:183], v[194:195], v[172:173]
	v_lshlrev_b32_e32 v172, 16, v174
	v_and_b32_e32 v173, 0xffff0000, v174
	v_lshlrev_b32_e32 v174, 16, v175
	v_and_b32_e32 v175, 0xffff0000, v175
	v_pk_fma_f32 v[180:181], v[180:181], v[192:193], v[184:185]
	v_pk_fma_f32 v[178:179], v[178:179], v[190:191], v[174:175]
	v_pk_fma_f32 v[176:177], v[176:177], v[188:189], v[172:173]
	v_add_co_u32_e32 v184, vcc, s7, v248
	v_cvt_pk_bf16_f32 v172, v180, v181
	v_cvt_pk_bf16_f32 v173, v182, v183
	v_cvt_pk_bf16_f32 v174, v176, v177
	v_cvt_pk_bf16_f32 v175, v178, v179
	v_addc_co_u32_e32 v185, vcc, 0, v249, vcc
	global_store_dwordx4 v[184:185], v[172:175], off offset:2048
	s_mov_b32 s7, 0x5b541000
	s_nop 0
	v_lshlrev_b32_e32 v172, 16, v160
	v_and_b32_e32 v173, 0xffff0000, v160
	v_lshlrev_b32_e32 v160, 16, v161
	v_and_b32_e32 v161, 0xffff0000, v161
	v_pk_fma_f32 v[170:171], v[170:171], v[182:183], v[160:161]
	v_lshlrev_b32_e32 v160, 16, v162
	v_and_b32_e32 v161, 0xffff0000, v162
	v_lshlrev_b32_e32 v162, 16, v163
	v_and_b32_e32 v163, 0xffff0000, v163
	v_pk_fma_f32 v[168:169], v[168:169], v[180:181], v[172:173]
	v_pk_fma_f32 v[166:167], v[166:167], v[178:179], v[162:163]
	v_pk_fma_f32 v[164:165], v[164:165], v[176:177], v[160:161]
	v_add_co_u32_e32 v172, vcc, s7, v248
	v_cvt_pk_bf16_f32 v160, v168, v169
	v_cvt_pk_bf16_f32 v161, v170, v171
	v_cvt_pk_bf16_f32 v162, v164, v165
	v_cvt_pk_bf16_f32 v163, v166, v167
	v_addc_co_u32_e32 v173, vcc, 0, v249, vcc
	global_store_dwordx4 v[172:173], v[160:163], off offset:2048
	s_mov_b32 s7, 0x5b549000
	s_nop 0
	v_lshlrev_b32_e32 v160, 16, v148
	v_and_b32_e32 v161, 0xffff0000, v148
	v_lshlrev_b32_e32 v148, 16, v149
	v_and_b32_e32 v149, 0xffff0000, v149
	v_pk_fma_f32 v[158:159], v[158:159], v[170:171], v[148:149]
	v_lshlrev_b32_e32 v148, 16, v150
	v_and_b32_e32 v149, 0xffff0000, v150
	v_lshlrev_b32_e32 v150, 16, v151
	v_and_b32_e32 v151, 0xffff0000, v151
	v_pk_fma_f32 v[156:157], v[156:157], v[168:169], v[160:161]
	v_pk_fma_f32 v[154:155], v[154:155], v[166:167], v[150:151]
	v_pk_fma_f32 v[152:153], v[152:153], v[164:165], v[148:149]
	v_add_co_u32_e32 v160, vcc, s7, v248
	v_cvt_pk_bf16_f32 v148, v156, v157
	v_cvt_pk_bf16_f32 v149, v158, v159
	v_cvt_pk_bf16_f32 v150, v152, v153
	v_cvt_pk_bf16_f32 v151, v154, v155
	v_addc_co_u32_e32 v161, vcc, 0, v249, vcc
	global_store_dwordx4 v[160:161], v[148:151], off offset:2048
	s_mov_b32 s7, 0x5b551000
	s_nop 0
	v_lshlrev_b32_e32 v148, 16, v136
	v_and_b32_e32 v149, 0xffff0000, v136
	v_lshlrev_b32_e32 v136, 16, v137
	v_and_b32_e32 v137, 0xffff0000, v137
	v_pk_fma_f32 v[146:147], v[146:147], v[158:159], v[136:137]
	v_lshlrev_b32_e32 v136, 16, v138
	v_and_b32_e32 v137, 0xffff0000, v138
	v_lshlrev_b32_e32 v138, 16, v139
	v_and_b32_e32 v139, 0xffff0000, v139
	v_pk_fma_f32 v[144:145], v[144:145], v[156:157], v[148:149]
	v_pk_fma_f32 v[142:143], v[142:143], v[154:155], v[138:139]
	v_pk_fma_f32 v[140:141], v[140:141], v[152:153], v[136:137]
	v_add_co_u32_e32 v148, vcc, s7, v248
	v_cvt_pk_bf16_f32 v136, v144, v145
	v_cvt_pk_bf16_f32 v137, v146, v147
	v_cvt_pk_bf16_f32 v138, v140, v141
	v_cvt_pk_bf16_f32 v139, v142, v143
	v_addc_co_u32_e32 v149, vcc, 0, v249, vcc
	global_store_dwordx4 v[148:149], v[136:139], off offset:2048
	s_nop 1
	v_lshlrev_b32_e32 v136, 16, v124
	v_and_b32_e32 v137, 0xffff0000, v124
	v_lshlrev_b32_e32 v124, 16, v125
	v_and_b32_e32 v125, 0xffff0000, v125
	v_pk_fma_f32 v[114:115], v[134:135], v[146:147], v[124:125]
	v_lshlrev_b32_e32 v124, 16, v126
	v_and_b32_e32 v125, 0xffff0000, v126
	v_lshlrev_b32_e32 v126, 16, v127
	v_and_b32_e32 v127, 0xffff0000, v127
	v_pk_fma_f32 v[112:113], v[132:133], v[144:145], v[136:137]
	v_pk_fma_f32 v[110:111], v[130:131], v[142:143], v[126:127]
	v_pk_fma_f32 v[108:109], v[128:129], v[140:141], v[124:125]
	v_readlane_b32 s6, v253, 62
	s_nop 1
	v_add_u32_e32 v1, s6, v1
	s_mov_b32 s6, 0x1ffff
	v_cmp_lt_i32_e32 vcc, s6, v1
	v_readlane_b32 s6, v254, 41
	s_or_b64 s[4:5], vcc, s[4:5]
	s_nop 0
	v_add_u32_e32 v2, s6, v2
	s_andn2_b64 exec, exec, s[4:5]
	s_cbranch_execnz .LBB0_705
.LBB0_708:
	s_or_b64 exec, exec, s[2:3]
	v_readlane_b32 s2, v254, 47
	s_add_i32 s33, s2, 3
	s_cmp_ge_i32 s33, s19
	s_cbranch_scc1 .LBB0_758
	s_waitcnt vmcnt(0)
	s_waitcnt lgkmcnt(0)
	s_barrier
	s_mov_b64 s[2:3], exec
	v_readlane_b32 s4, v254, 54
	v_readlane_b32 s5, v254, 55
	s_and_b64 s[4:5], s[2:3], s[4:5]
	s_mov_b64 exec, s[4:5]
	s_cbranch_execz .LBB0_757
	v_readlane_b32 s4, v251, 28
	s_waitcnt vmcnt(0) expcnt(0) lgkmcnt(0)
	s_nop 0
	v_mov_b32_e32 v1, s4
	ds_read_b32 v4, v1
	ds_read_b32 v2, v1 offset:4
	s_waitcnt lgkmcnt(1)
	v_cmp_ne_u32_e32 vcc, 0, v4
	s_cbranch_vccnz .LBB0_725
	v_readlane_b32 s6, v251, 8
	v_readlane_b32 s7, v251, 9
	s_load_dwordx2 s[4:5], s[6:7], 0x4
	s_mov_b32 s11, 1
	s_waitcnt lgkmcnt(0)
	s_mul_i32 s10, s4, s20
	s_mul_i32 s10, s10, s5
	s_branch .LBB0_713
.Ltramp_105:
	s_branch .LBB0_105
.LBB0_712:
	s_and_b64 vcc, exec, s[6:7]
	s_cbranch_vccnz .LBB0_720

.LBB0_1245:
	s_waitcnt vmcnt(0)
	buffer_inv sc1
	s_mov_b32 s14, 0x100001
	s_branch .LBB0_1247

.LBB0_1251:
	s_waitcnt vmcnt(0) lgkmcnt(0)
	s_nop 0

.LBB0_1361:
	s_waitcnt vmcnt(0)
	buffer_inv sc1
	s_mov_b32 s10, 0x100001
	s_branch .LBB0_1363
